# attention-hosted conversion: the 16 loads go out behind the QK MFMAs instead of behind the K reads
# baseline (speedup 1.0000x reference)
; __device__ __forceinline__ void phase_attn(Frame& F) {
;     ...
;         lds_barrier();
;         LAS unsigned char* kb = F.lds + buf * ABUF;
;         const bf16x8 q0 = qn0, q1 = qn1;
;         {
;             LAS unsigned char* ob = F.lds + (buf ^ 1) * ABUF;
; #pragma unroll
;             for (int jj = 0; jj < 4; ++jj) { const int ch = tid + 512 * jj, row = ch >> 3, c16 = ch & 7;
;                 *(LAS u32x4*)(ob + row * ATT_ROWB + c16 * 16) = kr[jj]; *(LAS u32x4*)(ob + ATT_VOFF + row * ATT_ROWB + c16 * 16) = vr[jj]; }
;         }
;         const AttnUnit nu = un;
;         un = attn_decode(x8 * PER_X + (jl + 2 * G8 < jlast ? jl + 2 * G8 : jlast)); attn_issue(qkv, un, tid, kr, vr);
;         { const char* qb = (const char*)qkv + (((size_t)nu.b * SEQ + nu.r) * NPROJ + nu.h * 64) * 2; const unsigned qo = __umul24((unsigned)(128 * nu.n + ql), (unsigned)nu.d * (NPROJ * 2)) + 16u * fq;
;           qn0 = *(const bf16x8*)(qb + qo); qn1 = *(const bf16x8*)(qb + qo + 64); }
;         const unsigned qrow = __umul24((unsigned)(128 * cu.n + ql), (unsigned)cu.d);
;         const float c1 = 0.125f * LOG2E;
;         const float nc2 = -__builtin_amdgcn_exp2f(-(float)(cu.h + 1)) * (float)cu.d * LOG2E;
;         const bool first = cu.n == 0;
;         f32x4 St[9];
;         const f32x4 eb = (f32x4){ef[0], ef[1], ef[2], ef[3]} * nc2;
;         float mx = -INFINITY;
;         bf16x8 kf[9][2];
; #pragma unroll
;         for (int T = 0; T < 9; ++T) { LAS unsigned char* ka = kb + (16 * (w + T) + fr) * ATT_ROWB + fq * 16; kf[T][0] = *(LAS bf16x8*)ka; kf[T][1] = *(LAS bf16x8*)(ka + 64); }
;         __builtin_amdgcn_sched_barrier(0);
; #pragma unroll
;         for (int T = 0; T < 9; ++T) {
;             f32x4 sa = (f32x4){0.f, 0.f, 0.f, 0.f};
;             sa = __builtin_amdgcn_mfma_f32_16x16x32_bf16(kf[T][0], q0, sa, 0, 0, 0);
;             sa = __builtin_amdgcn_mfma_f32_16x16x32_bf16(kf[T][1], q1, sa, 0, 0, 0);
;             const float kT = (!first || w + T >= 8) ? nc2 * (float)(128 - 16 * T) : -INFINITY;
;             sa = sa * c1 + (eb + kT);
; #pragma unroll
;             for (int rg = 0; rg < 4; ++rg) {
;                 if (T == 0) sa[rg] = ef[rg] <= 0.f ? sa[rg] : -INFINITY;
;                 if (T == 8) sa[rg] = ef[rg] >= 0.f ? sa[rg] : -INFINITY;
;             }
;             St[T] = sa;
;             mx = fmaxf(mx, fmaxf(fmaxf(sa[0], sa[1]), fmaxf(sa[2], sa[3])));
.Lcva_wd:
	v_mov_b64_e32 v[48:49], v[4:5]
	v_mov_b64_e32 v[46:47], v[2:3]
	v_mov_b64_e32 v[44:45], v[8:9]
	v_mov_b64_e32 v[42:43], v[6:7]
	s_lshl_b32 s65, 1, s35
	s_waitcnt lgkmcnt(0)
	s_barrier
	s_add_i32 s37, s30, 1
	v_cvt_f32_u32_e32 v54, s37
	v_cvt_f32_u32_e32 v55, s65
	v_add_u32_e32 v110, s85, v82
	v_add_u32_e32 v58, v110, v90
	v_exp_f32_e64 v54, -v54
	v_add_u32_e32 v66, v110, v91
	v_add_u32_e32 v74, v110, v92
	v_add_u32_e32 v111, v110, v93
	v_mul_f32_e32 v79, v55, v54
	ds_read_b128 v[54:57], v58
	ds_read_b128 v[58:61], v58 offset:64
	ds_read_b128 v[62:65], v66
	ds_read_b128 v[66:69], v66 offset:64
	ds_read_b128 v[70:73], v74
	ds_read_b128 v[74:77], v74 offset:64
	ds_read_b128 v[112:115], v111
	ds_read_b128 v[116:119], v111 offset:64
	v_add_u32_e32 v111, v110, v94
	ds_read_b128 v[120:123], v111
	ds_read_b128 v[124:127], v111 offset:64
	v_add_u32_e32 v111, v110, v95
	ds_read_b128 v[128:131], v111
	ds_read_b128 v[132:135], v111 offset:64
	v_add_u32_e32 v111, v110, v96
	ds_read_b128 v[136:139], v111
	ds_read_b128 v[140:143], v111 offset:64
	v_add_u32_e32 v111, v110, v97
	v_add_u32_e32 v110, v110, v98
	ds_read_b128 v[144:147], v111
	ds_read_b128 v[148:151], v111 offset:64
	ds_read_b128 v[152:155], v110
	ds_read_b128 v[156:159], v110 offset:64
	s_cmp_lg_u32 s64, 0
	v_lshl_add_u32 v78, s64, 7, v86
	s_cselect_b64 s[64:65], -1, 0
	v_mul_f32_e32 v160, 0xbfb8aa3b, v79
	v_and_b32_e32 v110, 0xffffff, v78
	s_waitcnt lgkmcnt(14)
	v_mfma_f32_16x16x32_bf16 v[54:57], v[54:57], v[46:49], 0
	v_mul_f32_e32 v78, 0x43000000, v160
	s_or_b64 vcc, s[64:65], s[38:39]
	v_cndmask_b32_e32 v78, v109, v78, vcc
	v_mfma_f32_16x16x32_bf16 v[54:57], v[58:61], v[42:45], v[54:57]
	v_fma_f32 v162, v50, v160, v78
	v_fma_f32 v163, v51, v160, v78
	v_pk_fma_f32 v[78:79], v[52:53], v[160:161], v[78:79] op_sel_hi:[1,0,0]
	s_or_b64 vcc, s[64:65], s[40:41]
	s_nop 3
	v_pk_fma_f32 v[56:57], v[56:57], s[56:57], v[78:79] op_sel_hi:[1,0,1]
	v_pk_fma_f32 v[54:55], v[54:55], s[56:57], v[162:163] op_sel_hi:[1,0,1]
	v_cndmask_b32_e64 v164, v109, v56, s[10:11]
	v_cndmask_b32_e64 v162, v109, v54, s[6:7]
	v_cndmask_b32_e64 v163, v109, v55, s[8:9]
	v_cndmask_b32_e64 v165, v109, v57, s[12:13]
	v_mfma_f32_16x16x32_bf16 v[54:57], v[62:65], v[46:49], 0
	v_max_f32_e32 v58, v162, v163
	v_max_f32_e32 v59, v164, v165
	v_max3_f32 v62, v58, v59, s78
	v_mfma_f32_16x16x32_bf16 v[54:57], v[66:69], v[42:45], v[54:57]
	v_mul_f32_e32 v58, 0x42e00000, v160
	v_cndmask_b32_e32 v58, v109, v58, vcc
	v_pk_fma_f32 v[60:61], v[50:51], v[160:161], v[58:59] op_sel_hi:[1,0,0]
	v_pk_fma_f32 v[58:59], v[52:53], v[160:161], v[58:59] op_sel_hi:[1,0,0]
	s_or_b64 vcc, s[64:65], s[42:43]
	s_nop 2
	v_pk_fma_f32 v[166:167], v[56:57], s[56:57], v[58:59] op_sel_hi:[1,0,1]
	s_waitcnt lgkmcnt(13)
	v_mfma_f32_16x16x32_bf16 v[56:59], v[70:73], v[46:49], 0
	v_fma_f32 v78, v54, s56, v60
	v_fma_f32 v79, v55, s56, v61
	v_max_f32_e32 v54, v166, v167
	v_max3_f32 v63, v78, v79, v54
	s_waitcnt lgkmcnt(12)
	v_mfma_f32_16x16x32_bf16 v[54:57], v[74:77], v[42:45], v[56:59]
	s_nop 2
	v_mul_f32_e32 v58, 0x42c00000, v160
	v_cndmask_b32_e32 v58, v109, v58, vcc
	v_pk_fma_f32 v[60:61], v[50:51], v[160:161], v[58:59] op_sel_hi:[1,0,0]
	v_pk_fma_f32 v[58:59], v[52:53], v[160:161], v[58:59] op_sel_hi:[1,0,0]
	s_nop 0
	v_pk_fma_f32 v[76:77], v[54:55], s[56:57], v[60:61] op_sel_hi:[1,0,1]
	v_pk_fma_f32 v[74:75], v[56:57], s[56:57], v[58:59] op_sel_hi:[1,0,1]
	s_waitcnt lgkmcnt(11)
	v_mfma_f32_16x16x32_bf16 v[54:57], v[112:115], v[46:49], 0
	v_max_f32_e32 v58, v74, v75
	v_max3_f32 v58, v76, v77, v58
	v_max3_f32 v62, v62, v63, v58
	s_waitcnt lgkmcnt(10)
	v_mfma_f32_16x16x32_bf16 v[54:57], v[116:119], v[42:45], v[54:57]
	v_mul_f32_e32 v58, 0x42a00000, v160
	s_or_b64 vcc, s[64:65], s[44:45]
	v_cndmask_b32_e32 v58, v109, v58, vcc
	v_pk_fma_f32 v[60:61], v[50:51], v[160:161], v[58:59] op_sel_hi:[1,0,0]
	v_pk_fma_f32 v[58:59], v[52:53], v[160:161], v[58:59] op_sel_hi:[1,0,0]
	s_nop 2
	v_pk_fma_f32 v[72:73], v[54:55], s[56:57], v[60:61] op_sel_hi:[1,0,1]
	v_pk_fma_f32 v[70:71], v[56:57], s[56:57], v[58:59] op_sel_hi:[1,0,1]
	s_waitcnt lgkmcnt(9)
	v_mfma_f32_16x16x32_bf16 v[56:59], v[120:123], v[46:49], 0
	v_max_f32_e32 v54, v70, v71
	v_max3_f32 v63, v72, v73, v54
	s_or_b64 vcc, s[64:65], s[46:47]
	s_waitcnt lgkmcnt(8)
	v_mfma_f32_16x16x32_bf16 v[54:57], v[124:127], v[42:45], v[56:59]
	s_nop 2
	v_mul_f32_e32 v58, 0x42800000, v160
	v_cndmask_b32_e32 v58, v109, v58, vcc
	v_pk_fma_f32 v[60:61], v[50:51], v[160:161], v[58:59] op_sel_hi:[1,0,0]
	v_pk_fma_f32 v[58:59], v[52:53], v[160:161], v[58:59] op_sel_hi:[1,0,0]
	s_nop 0
	v_pk_fma_f32 v[68:69], v[54:55], s[56:57], v[60:61] op_sel_hi:[1,0,1]
	v_pk_fma_f32 v[66:67], v[56:57], s[56:57], v[58:59] op_sel_hi:[1,0,1]
	s_waitcnt lgkmcnt(7)
	v_mfma_f32_16x16x32_bf16 v[54:57], v[128:131], v[46:49], 0
	v_max_f32_e32 v58, v66, v67
	v_max3_f32 v58, v68, v69, v58
	v_max3_f32 v111, v62, v63, v58
	s_waitcnt lgkmcnt(6)
	v_mfma_f32_16x16x32_bf16 v[54:57], v[132:135], v[42:45], v[54:57]
	v_mul_f32_e32 v58, 0x42400000, v160
	s_or_b64 vcc, s[64:65], s[48:49]
	v_cndmask_b32_e32 v58, v109, v58, vcc
	v_pk_fma_f32 v[60:61], v[50:51], v[160:161], v[58:59] op_sel_hi:[1,0,0]
	v_pk_fma_f32 v[58:59], v[52:53], v[160:161], v[58:59] op_sel_hi:[1,0,0]
	s_nop 2
	v_pk_fma_f32 v[64:65], v[54:55], s[56:57], v[60:61] op_sel_hi:[1,0,1]
	v_pk_fma_f32 v[62:63], v[56:57], s[56:57], v[58:59] op_sel_hi:[1,0,1]
	s_waitcnt lgkmcnt(5)
	v_mfma_f32_16x16x32_bf16 v[56:59], v[136:139], v[46:49], 0
	v_max_f32_e32 v54, v62, v63
	v_max3_f32 v112, v64, v65, v54
	s_or_b64 vcc, s[64:65], s[50:51]
	s_waitcnt lgkmcnt(4)
	v_mfma_f32_16x16x32_bf16 v[54:57], v[140:143], v[42:45], v[56:59]
	s_nop 2
	v_mul_f32_e32 v58, 0x42000000, v160
	v_cndmask_b32_e32 v58, v109, v58, vcc
	v_pk_fma_f32 v[60:61], v[50:51], v[160:161], v[58:59] op_sel_hi:[1,0,0]
	v_pk_fma_f32 v[58:59], v[52:53], v[160:161], v[58:59] op_sel_hi:[1,0,0]
	s_nop 0
	v_pk_fma_f32 v[60:61], v[54:55], s[56:57], v[60:61] op_sel_hi:[1,0,1]
	v_pk_fma_f32 v[58:59], v[56:57], s[56:57], v[58:59] op_sel_hi:[1,0,1]
	s_waitcnt lgkmcnt(3)
	v_mfma_f32_16x16x32_bf16 v[54:57], v[144:147], v[46:49], 0
	v_max_f32_e32 v113, v58, v59
	v_max3_f32 v113, v60, v61, v113
	v_max3_f32 v111, v111, v112, v113
	s_waitcnt lgkmcnt(1)
	v_mfma_f32_16x16x32_bf16 v[46:49], v[152:155], v[46:49], 0
	s_or_b64 vcc, s[64:65], s[52:53]
	v_add_u32_e32 v144, s85, v89
	v_add_u32_e32 v130, v144, v99
	v_mfma_f32_16x16x32_bf16 v[112:115], v[148:151], v[42:45], v[54:57]
	v_add_u32_e32 v140, v144, v100
	v_add_u32_e32 v145, v144, v101
	s_nop 0
	v_mul_f32_e32 v54, 0x41800000, v160
	s_waitcnt lgkmcnt(0)
	v_mfma_f32_16x16x32_bf16 v[42:45], v[156:159], v[42:45], v[46:49]
	s_sub_u32 s32, s32, 1
	s_cmp_lt_i32 s32, 0
	s_cbranch_scc0 .Lcva_none_l
	s_mov_b32 s32, 3
	s_cmp_eq_u32 s90, 0
	s_cbranch_scc1 .Lcva_none_l
	s_sub_u32 s90, s90, 1
	s_lshr_b32 s98, s89, 6
	s_and_b32 s99, s89, 63
	s_mul_hi_u32 s100, s98, 0xaaaaaaab
	s_lshr_b32 s100, s100, 1
	s_mul_i32 s101, s100, 3
	s_sub_u32 s101, s98, s101
	s_cmp_lt_u32 s100, 256
	s_cselect_b32 s98, 0, 3
	s_cselect_b32 s95, s100, 0
	s_add_u32 s98, s98, s101
	s_lshl_b32 s98, s98, 1
	v_readlane_b32 s96, v253, s98
	s_add_u32 s98, s98, 1
	v_readlane_b32 s97, v253, s98
	s_lshl_b32 s95, s95, 20
	s_nop 3
	s_add_u32 s96, s96, s95
	s_addc_u32 s97, s97, 0
	s_cmp_eq_u32 s101, 2
	s_cbranch_scc1 .Lcva_down_l
	s_lshr_b32 s95, s99, 3
	s_and_b32 s99, s99, 7
	s_lshl_b32 s98, s95, 17
	s_add_u32 s96, s96, s98
	s_addc_u32 s97, s97, 0
	s_lshl_b32 s98, s99, 7
	s_add_u32 s96, s96, s98
	s_addc_u32 s97, s97, 0
	s_lshl_b32 s100, s100, 19
	s_lshr_b32 s98, s99, 2
	s_lshl_b32 s98, s98, 18
	s_add_u32 s100, s100, s98
	s_and_b32 s98, s99, 3
	s_lshl_b32 s98, s98, 15
	s_add_u32 s100, s100, s98
	s_lshl_b32 s98, s101, 17
	s_add_u32 s100, s100, s98
	s_lshl_b32 s98, s95, 7
	s_add_u32 s100, s100, s98
	v_readlane_b32 s92, v253, 12
	v_readlane_b32 s93, v253, 13
	s_mov_b32 s94, 0xc3317218
	s_cmp_eq_u32 s101, 0
	s_cselect_b32 s94, 0xc2b8aa3b, s94
	s_nop 3
	s_add_u32 s92, s92, s100
	s_addc_u32 s93, s93, 0
	s_movk_i32 s95, 0x400
	s_movk_i32 s98, 0x400
	s_branch .Lcva_go_l

; #define LAS __attribute__((address_space(3)))
; __device__ __forceinline__ unsigned cvt_pk_bf16(float lo, float hi) { const f32x2_t v = {lo, hi}; return __builtin_bit_cast(unsigned, __builtin_convertvector(v, bf16x2_t)); }
; __device__ __forceinline__ float fast_exp2(float x) { return __builtin_amdgcn_exp2f(x); }
; __device__ __forceinline__ void phase_attn(Frame& F) {
;     ...
;             LAS unsigned char* ob = F.lds + (buf ^ 1) * ABUF;
; #pragma unroll
;             for (int jj = 0; jj < 4; ++jj) { const int ch = tid + 512 * jj, row = ch >> 3, c16 = ch & 7;
;                 *(LAS u32x4*)(ob + row * ATT_ROWB + c16 * 16) = kr[jj]; *(LAS u32x4*)(ob + ATT_VOFF + row * ATT_ROWB + c16 * 16) = vr[jj]; }
;         }
;         const AttnUnit nu = un;
;         un = attn_decode(x8 * PER_X + (jl + 2 * G8 < jlast ? jl + 2 * G8 : jlast)); attn_issue(qkv, un, tid, kr, vr);
;         { const char* qb = (const char*)qkv + (((size_t)nu.b * SEQ + nu.r) * NPROJ + nu.h * 64) * 2; const unsigned qo = __umul24((unsigned)(128 * nu.n + ql), (unsigned)nu.d * (NPROJ * 2)) + 16u * fq;
;           qn0 = *(const bf16x8*)(qb + qo); qn1 = *(const bf16x8*)(qb + qo + 64); }
;     ...
;         mx = fmaxf(mx, __shfl_xor(mx, 16)); mx = fmaxf(mx, __shfl_xor(mx, 32));
;         f32x4 lv = (f32x4){0.f, 0.f, 0.f, 0.f};
;         f32x4 nmx = (f32x4){-mx, -mx, -mx, -mx}; asm volatile("" : "+v"(nmx));
; #pragma unroll
;         for (int T = 0; T < 9; ++T) { const f32x4 d = St[T] + nmx; f32x4 pv; pv.x = fast_exp2(d.x); pv.y = fast_exp2(d.y); pv.z = fast_exp2(d.z); pv.w = fast_exp2(d.w); St[T] = pv; lv = lv + pv; }
;         float l = (lv.x + lv.y) + (lv.z + lv.w);
;         l += __shfl_xor(l, 16); l += __shfl_xor(l, 32);
;         f32x4 O[4];
; #pragma unroll
;         for (int dt = 0; dt < 4; ++dt) O[dt] = (f32x4){0.f, 0.f, 0.f, 0.f};
; #pragma unroll
;         for (int T = 0; T < 9; ++T) {
;             u32x2 pw; pw.x = cvt_pk_bf16(St[T][0], St[T][1]); pw.y = cvt_pk_bf16(St[T][2], St[T][3]);
;             const s16x4 pb = __builtin_bit_cast(s16x4, pw);
;             LAS unsigned char* va = kb + ATT_VOFF + (16 * (w + T) + 4 * fq + (fr >> 2)) * ATT_ROWB + (8 * (fr & 3)) * 2;
; #pragma unroll
;             for (int dt = 0; dt < 4; ++dt) O[dt] = __builtin_amdgcn_mfma_f32_16x16x16bf16_1k(tr_read(va + 64 * (dt >> 1) + 8 * (dt & 1)), pb, O[dt], 0, 0, 0);
.Lcva_none_l:
	s_add_i32 s37, s77, s70
	s_xor_b32 s79, s79, 1
	s_min_i32 s37, s37, s71
	s_mul_i32 s58, s79, 0x12000
	s_add_i32 s37, s37, s3
	v_add_u32_e32 v2, s58, v84
	s_mul_hi_i32 s58, s37, 0x2aaaaaab
	s_lshr_b32 s59, s58, 31
	s_ashr_i32 s58, s58, 4
	s_add_i32 s59, s58, s59
	s_mul_i32 s58, s59, 0x60
	s_sub_i32 s37, s37, s58
	s_ashr_i32 s58, s59, 3
	s_and_b32 s80, s59, 7
	v_add_u32_e32 v3, v2, v83
	s_cmp_gt_i32 s37, 31
	ds_write_b128 v3, v[38:41]
	ds_write_b128 v3, v[34:37] offset:36864
	v_add_u32_e32 v3, v2, v85
	s_cselect_b64 s[82:83], -1, 0
	s_cmp_gt_i32 s37, 63
	ds_write_b128 v3, v[30:33]
	ds_write_b128 v3, v[26:29] offset:36864
	v_add_u32_e32 v3, v2, v87
	v_add_u32_e32 v2, v2, v88
	s_cselect_b64 s[86:87], -1, 0
	ds_write_b128 v3, v[22:25]
	ds_write_b128 v3, v[18:21] offset:36864
	ds_write_b128 v2, v[14:17]
	ds_write_b128 v2, v[10:13] offset:36864
	v_cndmask_b32_e64 v2, 0, 1, s[86:87]
	s_cmp_lg_u64 s[82:83], 0
	v_readfirstlane_b32 s59, v2
	s_addc_u32 s81, s59, 0
	s_lshl_b32 s59, s81, 5
	s_lshl_b32 s82, s81, 1
	s_sub_i32 s37, s37, s59
	s_sub_i32 s59, 5, s82
	s_ashr_i32 s83, s37, s59
	s_lshl_b32 s59, -1, s59
	s_andn2_b32 s84, s37, s59
	s_ashr_i32 s59, s58, 31
	s_lshl_b64 s[86:87], s[58:59], 12
	s_ashr_i32 s37, s83, 31
	s_add_u32 s59, s86, s83
	s_addc_u32 s37, s87, s37
	s_mulk_i32 s37, 0xa00
	s_mul_hi_u32 s86, s59, 0xa00
	s_add_i32 s87, s86, s37
	s_mulk_i32 s59, 0xa00
	s_lshl_b32 s37, s80, 6
	s_or_b32 s86, s59, s37
	s_lshl_b64 s[86:87], s[86:87], 1
	s_add_u32 s37, s33, s86
	s_addc_u32 s59, s66, s87
	s_add_u32 s86, s37, 0x400
	s_addc_u32 s87, s59, 0
	s_lshl_b32 s59, s84, 7
	v_add_u32_e32 v2, s59, v81
	s_lshl_b32 s37, 0x1400, s82
	v_max_i32_e32 v3, 0, v2
	v_mul_u32_u24_e32 v3, s37, v3
	v_or_b32_e32 v3, v3, v80
	global_load_dwordx4 v[38:41], v3, s[86:87]
	global_load_dwordx4 v[34:37], v3, s[86:87] offset:1024
	v_max_i32_e32 v3, 0xffffffc0, v2
	v_add_u32_e32 v3, 64, v3
	v_mul_u32_u24_e32 v3, s37, v3
	v_or_b32_e32 v3, v3, v80
	global_load_dwordx4 v[30:33], v3, s[86:87]
	global_load_dwordx4 v[26:29], v3, s[86:87] offset:1024
	v_add_u32_e32 v3, s59, v1
	v_max_i32_e32 v2, 0xffffff40, v2
	v_max_i32_e32 v3, 0, v3
	v_add_u32_e32 v2, 0xc0, v2
	v_mul_u32_u24_e32 v3, s37, v3
	v_mul_u32_u24_e32 v2, s37, v2
	v_or_b32_e32 v3, v3, v80
	v_or_b32_e32 v2, v2, v80
	s_ashr_i32 s37, s36, 31
	global_load_dwordx4 v[22:25], v3, s[86:87]
	global_load_dwordx4 v[18:21], v3, s[86:87] offset:1024
	global_load_dwordx4 v[14:17], v2, s[86:87]
	global_load_dwordx4 v[10:13], v2, s[86:87] offset:1024
	s_lshl_b64 s[86:87], s[36:37], 12
	s_ashr_i32 s37, s73, 31
	s_add_u32 s59, s86, s73
	s_addc_u32 s37, s87, s37
	s_mulk_i32 s37, 0xa00
	s_mul_hi_u32 s86, s59, 0xa00
	s_add_i32 s87, s86, s37
	s_mulk_i32 s59, 0xa00
	s_lshl_b32 s37, s75, 6
	s_or_b32 s86, s59, s37
	s_lshl_b64 s[86:87], s[86:87], 1
	s_add_u32 s86, s33, s86
	s_addc_u32 s87, s66, s87
	s_lshl_b32 s37, 0x1400, s74
	v_lshl_add_u32 v2, s76, 7, v86
	s_and_b32 s37, s37, 0x555400
	v_mul_u32_u24_e32 v2, s37, v2
	v_or_b32_e32 v6, v2, v82
	global_load_dwordx4 v[2:5], v6, s[86:87]
	s_nop 0
	global_load_dwordx4 v[6:9], v6, s[86:87] offset:64
	v_cndmask_b32_e32 v54, v109, v54, vcc
	s_or_b64 vcc, s[64:65], s[54:55]
	v_pk_fma_f32 v[56:57], v[50:51], v[160:161], v[54:55] op_sel_hi:[1,0,0]
	v_mul_f32_e32 v46, 0, v160
	v_cndmask_b32_e32 v46, v109, v46, vcc
	v_pk_fma_f32 v[48:49], v[50:51], v[160:161], v[46:47] op_sel_hi:[1,0,0]
	v_pk_fma_f32 v[46:47], v[52:53], v[160:161], v[46:47] op_sel_hi:[1,0,0]
	v_pk_fma_f32 v[54:55], v[52:53], v[160:161], v[54:55] op_sel_hi:[1,0,0]
	v_pk_fma_f32 v[44:45], v[44:45], s[56:57], v[46:47] op_sel_hi:[1,0,1]
	v_pk_fma_f32 v[42:43], v[42:43], s[56:57], v[48:49] op_sel_hi:[1,0,1]
	v_cndmask_b32_e64 v48, v109, v44, s[18:19]
	v_and_b32_e32 v44, 64, v108
	v_pk_fma_f32 v[54:55], v[114:115], s[56:57], v[54:55] op_sel_hi:[1,0,1]
	v_cndmask_b32_e64 v47, v109, v43, s[16:17]
	v_cndmask_b32_e64 v49, v109, v45, s[20:21]
	v_xor_b32_e32 v43, 16, v108
	v_add_u32_e32 v44, 64, v44
	v_pk_fma_f32 v[56:57], v[112:113], s[56:57], v[56:57] op_sel_hi:[1,0,1]
	v_max_f32_e32 v112, v54, v55
	v_cndmask_b32_e64 v46, v109, v42, s[14:15]
	v_max_f32_e32 v42, v48, v49
	v_cmp_lt_i32_e32 vcc, v43, v44
	v_max3_f32 v112, v56, v57, v112
	v_max3_f32 v42, v46, v47, v42
	v_cndmask_b32_e32 v43, v108, v43, vcc
	v_max3_f32 v42, v111, v112, v42
	v_lshlrev_b32_e32 v142, 2, v43
	ds_bpermute_b32 v43, v142, v42
	s_waitcnt lgkmcnt(0)
	v_max_f32_e32 v43, v43, v43
	v_max_f32_e32 v42, v42, v43
	v_xor_b32_e32 v43, 32, v108
	v_cmp_lt_i32_e32 vcc, v43, v44
	s_nop 1
	v_cndmask_b32_e32 v43, v108, v43, vcc
	v_lshlrev_b32_e32 v143, 2, v43
	ds_bpermute_b32 v43, v143, v42
	s_waitcnt lgkmcnt(0)
	v_max_f32_e32 v43, v43, v43
	v_max_f32_e32 v111, v42, v43
	v_xor_b32_e32 v42, 0x80000000, v111
	v_mov_b32_e32 v43, v42
	v_mov_b32_e32 v44, v42
	v_mov_b32_e32 v45, v42
	ds_read_b64_tr_b16 v[120:121], v130 offset:36864
	v_pk_add_f32 v[118:119], v[166:167], v[44:45]
	v_pk_add_f32 v[112:113], v[164:165], v[44:45]
	v_exp_f32_e32 v126, v118
	v_exp_f32_e32 v127, v119
	ds_read_b64_tr_b16 v[118:119], v130 offset:36872
	v_pk_add_f32 v[114:115], v[162:163], v[42:43]
	v_exp_f32_e32 v112, v112
	v_exp_f32_e32 v114, v114
	v_exp_f32_e32 v113, v113
	v_exp_f32_e32 v115, v115
	ds_read_b64_tr_b16 v[128:129], v130 offset:36928
	ds_read_b64_tr_b16 v[130:131], v130 offset:36936
	v_pk_add_f32 v[134:135], v[76:77], v[42:43]
	v_cvt_pk_bf16_f32 v123, v112, v113
	v_cvt_pk_bf16_f32 v122, v114, v115
	v_pk_add_f32 v[116:117], v[112:113], 0 op_sel_hi:[1,0]
	v_pk_add_f32 v[124:125], v[114:115], 0 op_sel_hi:[1,0]
	s_waitcnt lgkmcnt(3)
; #define LAS __attribute__((address_space(3)))
; __device__ __forceinline__ unsigned cvt_pk_bf16(float lo, float hi) { const f32x2_t v = {lo, hi}; return __builtin_bit_cast(unsigned, __builtin_convertvector(v, bf16x2_t)); }
; __device__ __forceinline__ float fast_exp2(float x) { return __builtin_amdgcn_exp2f(x); }
; __device__ __forceinline__ s16x4 tr_read(LAS unsigned char* p) { return __builtin_bit_cast(s16x4, __builtin_amdgcn_ds_read_tr16_b64_v4i16((LAS s16x4*)p)); }
; __device__ __forceinline__ void phase_attn(Frame& F) {
;     ...
;         for (int T = 0; T < 9; ++T) { const f32x4 d = St[T] + nmx; f32x4 pv; pv.x = fast_exp2(d.x); pv.y = fast_exp2(d.y); pv.z = fast_exp2(d.z); pv.w = fast_exp2(d.w); St[T] = pv; lv = lv + pv; }
;         float l = (lv.x + lv.y) + (lv.z + lv.w);
;         l += __shfl_xor(l, 16); l += __shfl_xor(l, 32);
;         f32x4 O[4];
; #pragma unroll
;         for (int dt = 0; dt < 4; ++dt) O[dt] = (f32x4){0.f, 0.f, 0.f, 0.f};
; #pragma unroll
;         for (int T = 0; T < 9; ++T) {
;             u32x2 pw; pw.x = cvt_pk_bf16(St[T][0], St[T][1]); pw.y = cvt_pk_bf16(St[T][2], St[T][3]);
;             const s16x4 pb = __builtin_bit_cast(s16x4, pw);
;             LAS unsigned char* va = kb + ATT_VOFF + (16 * (w + T) + 4 * fq + (fr >> 2)) * ATT_ROWB + (8 * (fr & 3)) * 2;
; #pragma unroll
;             for (int dt = 0; dt < 4; ++dt) O[dt] = __builtin_amdgcn_mfma_f32_16x16x16bf16_1k(tr_read(va + 64 * (dt >> 1) + 8 * (dt & 1)), pb, O[dt], 0, 0, 0);
	v_mfma_f32_16x16x16_bf16 v[112:115], v[120:121], v[122:123], 0
	v_add_f32_e64 v120, v74, v44
	v_add_f32_e64 v121, v75, v45
	v_pk_add_f32 v[132:133], v[126:127], v[116:117]
	v_exp_f32_e32 v136, v120
	s_waitcnt lgkmcnt(2)
	v_mfma_f32_16x16x16_bf16 v[116:119], v[118:119], v[122:123], 0
	v_exp_f32_e32 v137, v121
	v_pk_add_f32 v[78:79], v[78:79], v[42:43]
	v_cvt_pk_bf16_f32 v139, v126, v127
	s_waitcnt lgkmcnt(1)
	v_mfma_f32_16x16x16_bf16 v[74:77], v[128:129], v[122:123], 0
	ds_read_b64_tr_b16 v[128:129], v140 offset:36864
	v_exp_f32_e32 v78, v78
	v_exp_f32_e32 v79, v79
	s_waitcnt lgkmcnt(1)
	v_mfma_f32_16x16x16_bf16 v[120:123], v[130:131], v[122:123], 0
	ds_read_b64_tr_b16 v[130:131], v140 offset:36872
	ds_read_b64_tr_b16 v[126:127], v140 offset:36928
	ds_read_b64_tr_b16 v[140:141], v140 offset:36936
	v_cvt_pk_bf16_f32 v138, v78, v79
	v_exp_f32_e32 v134, v134
	v_exp_f32_e32 v135, v135
	s_waitcnt lgkmcnt(3)
	v_mfma_f32_16x16x16_bf16 v[112:115], v[128:129], v[138:139], v[112:115]
	v_add_f32_e64 v128, v70, v44
	v_add_f32_e64 v129, v71, v45
	v_pk_add_f32 v[78:79], v[78:79], v[124:125]
	v_pk_add_f32 v[124:125], v[136:137], v[132:133]
	s_waitcnt lgkmcnt(2)
	v_mfma_f32_16x16x16_bf16 v[116:119], v[130:131], v[138:139], v[116:119]
	v_add_f32_e64 v130, v72, v42
	v_add_f32_e64 v131, v73, v43
	v_pk_add_f32 v[78:79], v[134:135], v[78:79]
	v_exp_f32_e32 v128, v128
	s_waitcnt lgkmcnt(1)
	v_mfma_f32_16x16x16_bf16 v[70:73], v[126:127], v[138:139], v[74:77]
	ds_read_b64_tr_b16 v[126:127], v145 offset:36864
	v_exp_f32_e32 v129, v129
	v_pk_add_f32 v[48:49], v[44:45], v[48:49]
	s_waitcnt lgkmcnt(1)
	v_mfma_f32_16x16x16_bf16 v[74:77], v[140:141], v[138:139], v[120:123]
	v_add_f32_e64 v124, v128, v124
	v_add_f32_e64 v125, v129, v125
	s_nop 0
	ds_read_b64_tr_b16 v[120:121], v145 offset:36872
	v_cvt_pk_bf16_f32 v122, v134, v135
	ds_read_b64_tr_b16 v[132:133], v145 offset:36928
	ds_read_b64_tr_b16 v[134:135], v145 offset:36936
	v_cvt_pk_bf16_f32 v123, v136, v137
	v_add_u32_e32 v136, v144, v102
	s_waitcnt lgkmcnt(3)
	v_mfma_f32_16x16x16_bf16 v[112:115], v[126:127], v[122:123], v[112:115]
	v_exp_f32_e32 v126, v130
	v_exp_f32_e32 v127, v131
	v_pk_add_f32 v[130:131], v[68:69], v[42:43]
	s_waitcnt lgkmcnt(2)
	v_mfma_f32_16x16x16_bf16 v[116:119], v[120:121], v[122:123], v[116:119]
	v_add_f32_e64 v120, v66, v44
	v_add_f32_e64 v121, v67, v45
	v_pk_add_f32 v[78:79], v[126:127], v[78:79]
	v_exp_f32_e32 v130, v130
	s_waitcnt lgkmcnt(1)
	v_mfma_f32_16x16x16_bf16 v[66:69], v[132:133], v[122:123], v[70:73]
	ds_read_b64_tr_b16 v[132:133], v136 offset:36864
	v_exp_f32_e32 v120, v120
	v_exp_f32_e32 v121, v121
	s_waitcnt lgkmcnt(1)
	v_mfma_f32_16x16x16_bf16 v[70:73], v[134:135], v[122:123], v[74:77]
	ds_read_b64_tr_b16 v[122:123], v136 offset:36872
	v_cvt_pk_bf16_f32 v134, v126, v127
	v_cvt_pk_bf16_f32 v135, v128, v129
	ds_read_b64_tr_b16 v[128:129], v136 offset:36928
	ds_read_b64_tr_b16 v[136:137], v136 offset:36936
	s_waitcnt lgkmcnt(3)
	v_mfma_f32_16x16x16_bf16 v[74:77], v[132:133], v[134:135], v[112:115]
	v_add_u32_e32 v132, v144, v103
	ds_read_b64_tr_b16 v[126:127], v132 offset:36872
	v_exp_f32_e32 v131, v131
	s_waitcnt lgkmcnt(3)
	v_mfma_f32_16x16x16_bf16 v[112:115], v[122:123], v[134:135], v[116:119]
	ds_read_b64_tr_b16 v[122:123], v132 offset:36864
	v_pk_add_f32 v[124:125], v[120:121], v[124:125]
	v_pk_add_f32 v[78:79], v[130:131], v[78:79]
	v_pk_add_f32 v[116:117], v[62:63], v[44:45]
	v_pk_add_f32 v[118:119], v[64:65], v[42:43]
	s_waitcnt lgkmcnt(3)
	v_mfma_f32_16x16x16_bf16 v[62:65], v[128:129], v[134:135], v[66:69]
	v_exp_f32_e32 v116, v116
	v_exp_f32_e32 v117, v117
	v_cvt_pk_bf16_f32 v128, v130, v131
	v_cvt_pk_bf16_f32 v129, v120, v121
	ds_read_b64_tr_b16 v[120:121], v132 offset:36928
	ds_read_b64_tr_b16 v[130:131], v132 offset:36936
	v_add_u32_e32 v132, v144, v104
	s_waitcnt lgkmcnt(4)
	v_mfma_f32_16x16x16_bf16 v[66:69], v[136:137], v[134:135], v[70:73]
	v_exp_f32_e32 v118, v118
	v_exp_f32_e32 v119, v119
	s_waitcnt lgkmcnt(2)
	v_mfma_f32_16x16x16_bf16 v[70:73], v[122:123], v[128:129], v[74:77]
	v_add_f32_e64 v122, v116, v124
	v_add_f32_e64 v123, v117, v125
	ds_read_b64_tr_b16 v[124:125], v132 offset:36872
	v_pk_add_f32 v[78:79], v[118:119], v[78:79]
	v_mfma_f32_16x16x16_bf16 v[74:77], v[126:127], v[128:129], v[112:115]
	v_cvt_pk_bf16_f32 v127, v116, v117
	v_cvt_pk_bf16_f32 v126, v118, v119
	s_nop 0
	v_pk_add_f32 v[112:113], v[58:59], v[44:45]
	v_pk_add_f32 v[114:115], v[60:61], v[42:43]
	s_waitcnt lgkmcnt(2)
	v_mfma_f32_16x16x16_bf16 v[58:61], v[120:121], v[128:129], v[62:65]
	ds_read_b64_tr_b16 v[120:121], v132 offset:36864
	v_exp_f32_e32 v112, v112
	v_exp_f32_e32 v113, v113
	v_exp_f32_e32 v114, v114
	s_waitcnt lgkmcnt(2)
	v_mfma_f32_16x16x16_bf16 v[62:65], v[130:131], v[128:129], v[66:69]
	ds_read_b64_tr_b16 v[116:117], v132 offset:36928
	ds_read_b64_tr_b16 v[128:129], v132 offset:36936
	v_exp_f32_e32 v115, v115
	v_pk_add_f32 v[118:119], v[112:113], v[122:123]
	v_add_u32_e32 v122, v144, v105
	s_waitcnt lgkmcnt(2)
	v_mfma_f32_16x16x16_bf16 v[66:69], v[120:121], v[126:127], v[70:73]
	ds_read_b64_tr_b16 v[120:121], v122 offset:36872
	v_mfma_f32_16x16x16_bf16 v[70:73], v[124:125], v[126:127], v[74:77]
	s_nop 2
	v_add_f32_e64 v74, v114, v78
	v_add_f32_e64 v75, v115, v79
	v_pk_add_f32 v[76:77], v[54:55], v[44:45]
	v_pk_add_f32 v[78:79], v[56:57], v[42:43]
	s_waitcnt lgkmcnt(2)
	v_mfma_f32_16x16x16_bf16 v[54:57], v[116:117], v[126:127], v[58:61]
	ds_read_b64_tr_b16 v[116:117], v122 offset:36864
	v_cvt_pk_bf16_f32 v114, v114, v115
	v_cvt_pk_bf16_f32 v115, v112, v113
	ds_read_b64_tr_b16 v[112:113], v122 offset:36928
	ds_read_b64_tr_b16 v[122:123], v122 offset:36936
	s_waitcnt lgkmcnt(4)
; #define LAS __attribute__((address_space(3)))
; __device__ __forceinline__ unsigned cvt_pk_bf16(float lo, float hi) { const f32x2_t v = {lo, hi}; return __builtin_bit_cast(unsigned, __builtin_convertvector(v, bf16x2_t)); }
; __device__ __forceinline__ s16x4 tr_read(LAS unsigned char* p) { return __builtin_bit_cast(s16x4, __builtin_amdgcn_ds_read_tr16_b64_v4i16((LAS s16x4*)p)); }
; __device__ __forceinline__ void phase_attn(Frame& F) {
;     ...
;         for (int T = 0; T < 9; ++T) {
;             u32x2 pw; pw.x = cvt_pk_bf16(St[T][0], St[T][1]); pw.y = cvt_pk_bf16(St[T][2], St[T][3]);
;             const s16x4 pb = __builtin_bit_cast(s16x4, pw);
;             LAS unsigned char* va = kb + ATT_VOFF + (16 * (w + T) + 4 * fq + (fr >> 2)) * ATT_ROWB + (8 * (fr & 3)) * 2;
; #pragma unroll
;             for (int dt = 0; dt < 4; ++dt) O[dt] = __builtin_amdgcn_mfma_f32_16x16x16bf16_1k(tr_read(va + 64 * (dt >> 1) + 8 * (dt & 1)), pb, O[dt], 0, 0, 0);
;         }
;         const float inv = 1.f / l;
;         bf16_t* op = (bf16_t*)((char*)part + (((size_t)cu.dsel * NTOK + (size_t)cu.b * SEQ + cu.r) * 512 + cu.h * 64) * 2 + (qrow * 1024u + 16u * fq));
; #pragma unroll
;         for (int u2 = 0; u2 < 2; ++u2) { u32x4 o4; o4.x = cvt_pk_bf16(O[2 * u2][0] * inv, O[2 * u2][1] * inv); o4.y = cvt_pk_bf16(O[2 * u2][2] * inv, O[2 * u2][3] * inv);
;             o4.z = cvt_pk_bf16(O[2 * u2 + 1][0] * inv, O[2 * u2 + 1][1] * inv); o4.w = cvt_pk_bf16(O[2 * u2 + 1][2] * inv, O[2 * u2 + 1][3] * inv); *(u32x4*)(op + 32 * u2) = o4; }
;         if (fq == 0) *(float*)((char*)lse + (((size_t)cu.dsel * NTOK + (size_t)cu.b * SEQ + cu.r) * 8 + cu.h) * 4 + qrow * 32u) = mx + __builtin_amdgcn_logf(l);
	v_mfma_f32_16x16x16_bf16 v[58:61], v[128:129], v[126:127], v[62:65]
	v_exp_f32_e32 v76, v76
	v_exp_f32_e32 v77, v77
	v_exp_f32_e32 v78, v78
	s_waitcnt lgkmcnt(2)
	v_mfma_f32_16x16x16_bf16 v[62:65], v[116:117], v[114:115], v[66:69]
	v_exp_f32_e32 v79, v79
	v_pk_add_f32 v[116:117], v[76:77], v[118:119]
	v_mfma_f32_16x16x16_bf16 v[66:69], v[120:121], v[114:115], v[70:73]
	s_nop 2
	v_add_f32_e64 v70, v42, v46
	v_add_f32_e64 v71, v43, v47
	s_waitcnt lgkmcnt(1)
	v_mfma_f32_16x16x16_bf16 v[42:45], v[112:113], v[114:115], v[54:57]
	v_exp_f32_e32 v72, v48
	v_exp_f32_e32 v73, v49
	v_exp_f32_e32 v70, v70
	v_add_u32_e32 v56, v144, v106
	ds_read_b64_tr_b16 v[54:55], v56 offset:36864
	s_waitcnt lgkmcnt(1)
	v_mfma_f32_16x16x16_bf16 v[46:49], v[122:123], v[114:115], v[58:61]
	v_exp_f32_e32 v71, v71
	v_cvt_pk_bf16_f32 v112, v78, v79
	v_cvt_pk_bf16_f32 v113, v76, v77
	ds_read_b64_tr_b16 v[58:59], v56 offset:36872
	ds_read_b64_tr_b16 v[76:77], v56 offset:36928
	ds_read_b64_tr_b16 v[114:115], v56 offset:36936
	s_waitcnt lgkmcnt(3)
	v_mfma_f32_16x16x16_bf16 v[54:57], v[54:55], v[112:113], v[62:65]
	s_nop 2
	v_add_f32_e64 v62, v78, v74
	v_add_f32_e64 v63, v79, v75
	v_pk_add_f32 v[64:65], v[72:73], v[116:117]
	v_pk_add_f32 v[62:63], v[70:71], v[62:63]
	v_add_u32_e32 v74, v144, v107
	s_waitcnt lgkmcnt(2)
	v_mfma_f32_16x16x16_bf16 v[58:61], v[58:59], v[112:113], v[66:69]
	s_nop 2
	v_pk_mov_b32 v[66:67], v[62:63], v[64:65] op_sel:[1,0]
	v_mov_b32_e32 v63, v65
	ds_read_b64_tr_b16 v[64:65], v74 offset:36864
	v_pk_add_f32 v[62:63], v[66:67], v[62:63]
	v_cvt_pk_bf16_f32 v66, v70, v71
	v_add_f32_e32 v75, v62, v63
	v_cvt_pk_bf16_f32 v67, v72, v73
	s_waitcnt lgkmcnt(2)
	v_mfma_f32_16x16x16_bf16 v[42:45], v[76:77], v[112:113], v[42:45]
	ds_read_b64_tr_b16 v[62:63], v74 offset:36872
	ds_read_b64_tr_b16 v[68:69], v74 offset:36928
	ds_read_b64_tr_b16 v[70:71], v74 offset:36936
	s_waitcnt lgkmcnt(3)
	v_mfma_f32_16x16x16_bf16 v[54:57], v[64:65], v[66:67], v[54:57]
	ds_bpermute_b32 v64, v142, v75
	s_waitcnt lgkmcnt(0)
	v_add_f32_e32 v72, v75, v64
	ds_bpermute_b32 v73, v143, v72
	v_mfma_f32_16x16x16_bf16 v[58:61], v[62:63], v[66:67], v[58:61]
	v_mfma_f32_16x16x16_bf16 v[62:65], v[68:69], v[66:67], v[42:45]
	s_waitcnt lgkmcnt(0)
	s_nop 1
	v_add_f32_e32 v43, v72, v73
	v_div_scale_f32 v68, s[64:65], v43, v43, 1.0
	v_mfma_f32_16x16x16_bf16 v[46:49], v[114:115], v[112:113], v[46:49]
	v_rcp_f32_e32 v69, v68
	v_lshlrev_b32_e32 v42, s35, v110
	s_ashr_i32 s35, s34, 31
	v_mfma_f32_16x16x16_bf16 v[44:47], v[70:71], v[66:67], v[46:49]
	s_lshl_b64 s[64:65], s[26:27], 16
	s_lshl_b64 s[34:35], s[34:35], 12
	s_ashr_i32 s26, s31, 31
	s_nop 0
	v_fma_f32 v48, -v68, v69, 1.0
	v_fmac_f32_e32 v69, v48, v69
	v_div_scale_f32 v48, vcc, 1.0, v43, 1.0
	v_mul_f32_e32 v49, v48, v69
	s_add_u32 s31, s34, s31
	v_fma_f32 v66, -v68, v49, v48
	s_addc_u32 s26, s35, s26
	v_fmac_f32_e32 v49, v66, v69
	s_add_u32 s34, s31, s64
	v_fma_f32 v48, -v68, v49, v48
	s_addc_u32 s35, s26, s65
	v_div_fmas_f32 v48, v48, v69, v49
	s_lshl_b32 s26, s30, 7
	s_lshl_b64 s[64:65], s[34:35], 10
	v_div_fixup_f32 v48, v48, v43, 1.0
	s_add_u32 s31, s24, s64
	v_lshl_or_b32 v49, v42, 10, v82
	s_addc_u32 s37, s25, s65
	v_pk_mul_f32 v[54:55], v[48:49], v[54:55] op_sel_hi:[0,1]
	v_pk_mul_f32 v[56:57], v[48:49], v[56:57] op_sel_hi:[0,1]
	s_add_u32 s64, s31, s26
	v_cvt_pk_bf16_f32 v54, v54, v55
	v_cvt_pk_bf16_f32 v55, v56, v57
	v_pk_mul_f32 v[56:57], v[48:49], v[58:59] op_sel_hi:[0,1]
	v_pk_mul_f32 v[58:59], v[48:49], v[60:61] op_sel_hi:[0,1]
	s_addc_u32 s65, s37, 0
	v_cvt_pk_bf16_f32 v56, v56, v57
	v_cvt_pk_bf16_f32 v57, v58, v59
	global_store_dwordx4 v49, v[54:57], s[64:65]
	v_pk_mul_f32 v[44:45], v[48:49], v[44:45] op_sel_hi:[0,1]
	s_nop 0
	v_pk_mul_f32 v[54:55], v[48:49], v[62:63] op_sel_hi:[0,1]
	v_pk_mul_f32 v[56:57], v[48:49], v[64:65] op_sel_hi:[0,1]
	v_cvt_pk_bf16_f32 v54, v54, v55
	v_cvt_pk_bf16_f32 v55, v56, v57
	v_cvt_pk_bf16_f32 v56, v44, v45
	v_pk_mul_f32 v[44:45], v[48:49], v[46:47] op_sel_hi:[0,1]
	v_cvt_pk_bf16_f32 v57, v44, v45
	global_store_dwordx4 v49, v[54:57], s[64:65] offset:64
	s_cmp_eq_u32 s95, 0
	s_cbranch_scc1 .Lcva_skip_l
; #define LAS __attribute__((address_space(3)))
; __device__ __forceinline__ void titem_finish(const TItem& t, int lane, const LAS unsigned char* buf) {
;     ...
;     const float wsc = t.scale;
; #pragma unroll
;     for (int j = 0; j < 4; ++j) { const int n = (lane >> 3) + 8 * j; const LAS float* s = sb + (8 * c) * 32 + 4 * ((n >> 2) ^ c) + (n & 3);
; #pragma unroll
;         for (int q = 0; q < 8; ++q) v[j][q] = s[32 * q] * wsc; }
;     if (t.f8) {
; #pragma unroll
;         for (int j = 0; j < 4; ++j) { const int n = (lane >> 3) + 8 * j;
;             int w0 = __builtin_amdgcn_cvt_pk_fp8_f32(v[j][0], v[j][1], 0, false); w0 = __builtin_amdgcn_cvt_pk_fp8_f32(v[j][2], v[j][3], w0, true);
;             int w1 = __builtin_amdgcn_cvt_pk_fp8_f32(v[j][4], v[j][5], 0, false); w1 = __builtin_amdgcn_cvt_pk_fp8_f32(v[j][6], v[j][7], w1, true);
;             u32x2 o; o.x = (unsigned)w0; o.y = (unsigned)w1;
;             __builtin_nontemporal_store(o, (u32x2*)((unsigned char*)t.WT + (size_t)(d0 + n) * t.K + k0 + 8 * c)); }
	s_waitcnt vmcnt(12)
	v_pk_mul_f32 v[168:169], v[168:169], s[94:95] op_sel_hi:[1,0]
	v_pk_mul_f32 v[170:171], v[170:171], s[94:95] op_sel_hi:[1,0]
	v_pk_mul_f32 v[172:173], v[172:173], s[94:95] op_sel_hi:[1,0]
	v_pk_mul_f32 v[174:175], v[174:175], s[94:95] op_sel_hi:[1,0]
	v_pk_mul_f32 v[176:177], v[176:177], s[94:95] op_sel_hi:[1,0]
	v_pk_mul_f32 v[178:179], v[178:179], s[94:95] op_sel_hi:[1,0]
	v_pk_mul_f32 v[180:181], v[180:181], s[94:95] op_sel_hi:[1,0]
	v_pk_mul_f32 v[182:183], v[182:183], s[94:95] op_sel_hi:[1,0]
	v_pk_mul_f32 v[184:185], v[184:185], s[94:95] op_sel_hi:[1,0]
	v_pk_mul_f32 v[186:187], v[186:187], s[94:95] op_sel_hi:[1,0]
	v_pk_mul_f32 v[188:189], v[188:189], s[94:95] op_sel_hi:[1,0]
	v_pk_mul_f32 v[190:191], v[190:191], s[94:95] op_sel_hi:[1,0]
	v_pk_mul_f32 v[192:193], v[192:193], s[94:95] op_sel_hi:[1,0]
	v_pk_mul_f32 v[194:195], v[194:195], s[94:95] op_sel_hi:[1,0]
	v_pk_mul_f32 v[196:197], v[196:197], s[94:95] op_sel_hi:[1,0]
	v_pk_mul_f32 v[198:199], v[198:199], s[94:95] op_sel_hi:[1,0]
	v_pk_mul_f32 v[200:201], v[200:201], s[94:95] op_sel_hi:[1,0]
	v_pk_mul_f32 v[202:203], v[202:203], s[94:95] op_sel_hi:[1,0]
	v_pk_mul_f32 v[204:205], v[204:205], s[94:95] op_sel_hi:[1,0]
	v_pk_mul_f32 v[206:207], v[206:207], s[94:95] op_sel_hi:[1,0]
	v_pk_mul_f32 v[208:209], v[208:209], s[94:95] op_sel_hi:[1,0]
	v_pk_mul_f32 v[210:211], v[210:211], s[94:95] op_sel_hi:[1,0]
	v_pk_mul_f32 v[212:213], v[212:213], s[94:95] op_sel_hi:[1,0]
	v_pk_mul_f32 v[214:215], v[214:215], s[94:95] op_sel_hi:[1,0]
	v_pk_mul_f32 v[216:217], v[216:217], s[94:95] op_sel_hi:[1,0]
	v_pk_mul_f32 v[218:219], v[218:219], s[94:95] op_sel_hi:[1,0]
	v_pk_mul_f32 v[220:221], v[220:221], s[94:95] op_sel_hi:[1,0]
	v_pk_mul_f32 v[222:223], v[222:223], s[94:95] op_sel_hi:[1,0]
	v_pk_mul_f32 v[224:225], v[224:225], s[94:95] op_sel_hi:[1,0]
	v_pk_mul_f32 v[226:227], v[226:227], s[94:95] op_sel_hi:[1,0]
	v_pk_mul_f32 v[228:229], v[228:229], s[94:95] op_sel_hi:[1,0]
	v_pk_mul_f32 v[230:231], v[230:231], s[94:95] op_sel_hi:[1,0]
	s_lshr_b32 s99, s95, 2
	v_lshlrev_b32_e32 v250, 4, v248
	v_cvt_pk_fp8_f32 v232, v168, v172
	v_cvt_pk_fp8_f32 v233, v184, v188
	v_cvt_pk_fp8_f32 v234, v200, v204
	v_cvt_pk_fp8_f32 v235, v216, v220
	v_cvt_pk_fp8_f32 v236, v169, v173
	v_cvt_pk_fp8_f32 v237, v185, v189
	v_cvt_pk_fp8_f32 v238, v201, v205
	v_cvt_pk_fp8_f32 v239, v217, v221
	v_cvt_pk_fp8_f32 v240, v170, v174
	v_cvt_pk_fp8_f32 v241, v186, v190
	v_cvt_pk_fp8_f32 v242, v202, v206
	v_cvt_pk_fp8_f32 v243, v218, v222
	v_cvt_pk_fp8_f32 v244, v171, v175
	v_cvt_pk_fp8_f32 v245, v187, v191
	v_cvt_pk_fp8_f32 v246, v203, v207
	v_cvt_pk_fp8_f32 v247, v219, v223
	v_mad_u32_u24 v250, v249, s99, v250
	v_add_u32_e32 v251, s95, v250
	v_add_u32_e32 v254, s95, v251
	v_add_u32_e32 v255, s95, v254
	v_cvt_pk_fp8_f32 v232, v176, v180 op_sel:[0,0,1]
	v_cvt_pk_fp8_f32 v233, v192, v196 op_sel:[0,0,1]
	v_cvt_pk_fp8_f32 v234, v208, v212 op_sel:[0,0,1]
	v_cvt_pk_fp8_f32 v235, v224, v228 op_sel:[0,0,1]
	v_cvt_pk_fp8_f32 v236, v177, v181 op_sel:[0,0,1]
	v_cvt_pk_fp8_f32 v237, v193, v197 op_sel:[0,0,1]
	v_cvt_pk_fp8_f32 v238, v209, v213 op_sel:[0,0,1]
	v_cvt_pk_fp8_f32 v239, v225, v229 op_sel:[0,0,1]
	v_cvt_pk_fp8_f32 v240, v178, v182 op_sel:[0,0,1]
	v_cvt_pk_fp8_f32 v241, v194, v198 op_sel:[0,0,1]
	v_cvt_pk_fp8_f32 v242, v210, v214 op_sel:[0,0,1]
	v_cvt_pk_fp8_f32 v243, v226, v230 op_sel:[0,0,1]
	v_cvt_pk_fp8_f32 v244, v179, v183 op_sel:[0,0,1]
	v_cvt_pk_fp8_f32 v245, v195, v199 op_sel:[0,0,1]
	v_cvt_pk_fp8_f32 v246, v211, v215 op_sel:[0,0,1]
	v_cvt_pk_fp8_f32 v247, v227, v231 op_sel:[0,0,1]
	global_store_dwordx4 v250, v[232:235], s[92:93] nt
	global_store_dwordx4 v251, v[236:239], s[92:93] nt
	global_store_dwordx4 v254, v[240:243], s[92:93] nt
	global_store_dwordx4 v255, v[244:247], s[92:93] nt
